# P0a: column-maxima items (w_in/w_out/w_query) rewritten by hand: all 32 row loads of an item in flight at once instead of serialized 2-load round trips
# speedup vs baseline: 1.1773x; 1.1773x over previous
; DI void p0_colmaxq_item(Frame& F, int item) {
;     const int lane = F.lane, nblk = D / 32, kb = item / nblk, nb = item % nblk, k0 = 64 * kb, n0 = 32 * nb;
;     float m = 0.f;
; #pragma unroll 8
;     for (int i = 0; i < 32; ++i) { const int kk = 2 * i + (lane >> 5); m = fmaxf(m, fabsf(F.wq[(size_t)(k0 + kk) * D + n0 + (lane & 31)])); }
;     m = fmaxf(m, __shfl_xor(m, 32));
;     if (lane < 32) F.CMAXQ[(size_t)kb * D + n0 + lane] = m;
; }
; DI void p0a_phase(Frame& F) {
;     ...
;         for (int r0 = nB > 0 ? gw - I_ADA : gw; r0 < NSMALL; r0 += nB > 0 ? nB : NGW) {
;             int r = r0;
;             if (r < I_WIN) { p0_colmax_item(F, r); continue; } r -= I_WIN;
;             if (r < I_WO) { p0_colmaxo_item(F, r); continue; } r -= I_WO;
;             p0_colmaxq_item(F, r);
.LBB0_22:
	s_lshl_b32 s0, s44, 2
	s_lshl_b32 s2, s33, 5
	s_and_b32 s47, s33, 0x7c0
	s_and_b32 s48, s0, 0x1f80
	s_mov_b32 s0, s2
	v_writelane_b32 v252, s0, 53
	s_and_b32 s49, s2, 0x7e0
	v_or_b32_e32 v25, s47, v46
	v_writelane_b32 v252, s1, 54
	s_cmpk_gt_u32 s33, 0x1fff
	s_mov_b64 s[0:1], -1
	s_waitcnt lgkmcnt(0)
	v_add_u32_e32 v12, 4, v25
	v_add_u32_e32 v14, 8, v25
	v_add_u32_e32 v16, 12, v25
	v_add_u32_e32 v18, 16, v25
	v_add_u32_e32 v20, 20, v25
	v_add_u32_e32 v22, 24, v25
	v_add_u32_e32 v24, 28, v25
	s_cbranch_scc0 .LBB0_78
	v_readfirstlane_b32 s2, v4
	v_readfirstlane_b32 s3, v5
	s_lshl_b32 s0, s49, 2
	s_lshl_b32 s4, s47, 13
	s_add_i32 s0, s0, s4
	s_add_u32 s0, s2, s0
	s_addc_u32 s1, s3, 0
	v_and_b32_e32 v1, 31, v148
	v_lshlrev_b32_e32 v1, 2, v1
	v_lshl_or_b32 v2, v46, 13, v1
	global_load_dword v12, v2, s[0:1]
	s_add_u32 s0, s0, 0x4000
	s_addc_u32 s1, s1, 0
	global_load_dword v13, v2, s[0:1]
	s_add_u32 s0, s0, 0x4000
	s_addc_u32 s1, s1, 0
	global_load_dword v14, v2, s[0:1]
	s_add_u32 s0, s0, 0x4000
	s_addc_u32 s1, s1, 0
	global_load_dword v15, v2, s[0:1]
	s_add_u32 s0, s0, 0x4000
	s_addc_u32 s1, s1, 0
	global_load_dword v16, v2, s[0:1]
	s_add_u32 s0, s0, 0x4000
	s_addc_u32 s1, s1, 0
	global_load_dword v17, v2, s[0:1]
	s_add_u32 s0, s0, 0x4000
	s_addc_u32 s1, s1, 0
	global_load_dword v18, v2, s[0:1]
	s_add_u32 s0, s0, 0x4000
	s_addc_u32 s1, s1, 0
	global_load_dword v19, v2, s[0:1]
	s_add_u32 s0, s0, 0x4000
	s_addc_u32 s1, s1, 0
	global_load_dword v20, v2, s[0:1]
	s_add_u32 s0, s0, 0x4000
	s_addc_u32 s1, s1, 0
	global_load_dword v21, v2, s[0:1]
	s_add_u32 s0, s0, 0x4000
	s_addc_u32 s1, s1, 0
	global_load_dword v22, v2, s[0:1]
	s_add_u32 s0, s0, 0x4000
	s_addc_u32 s1, s1, 0
	global_load_dword v23, v2, s[0:1]
	s_add_u32 s0, s0, 0x4000
	s_addc_u32 s1, s1, 0
	global_load_dword v24, v2, s[0:1]
	s_add_u32 s0, s0, 0x4000
	s_addc_u32 s1, s1, 0
	global_load_dword v25, v2, s[0:1]
	s_add_u32 s0, s0, 0x4000
	s_addc_u32 s1, s1, 0
	global_load_dword v26, v2, s[0:1]
	s_add_u32 s0, s0, 0x4000
	s_addc_u32 s1, s1, 0
	global_load_dword v27, v2, s[0:1]
	s_add_u32 s0, s0, 0x4000
	s_addc_u32 s1, s1, 0
	global_load_dword v28, v2, s[0:1]
	s_add_u32 s0, s0, 0x4000
	s_addc_u32 s1, s1, 0
	global_load_dword v29, v2, s[0:1]
	s_add_u32 s0, s0, 0x4000
	s_addc_u32 s1, s1, 0
	global_load_dword v30, v2, s[0:1]
	s_add_u32 s0, s0, 0x4000
	s_addc_u32 s1, s1, 0
	global_load_dword v31, v2, s[0:1]
	s_add_u32 s0, s0, 0x4000
	s_addc_u32 s1, s1, 0
	global_load_dword v32, v2, s[0:1]
	s_add_u32 s0, s0, 0x4000
	s_addc_u32 s1, s1, 0
	global_load_dword v33, v2, s[0:1]
	s_add_u32 s0, s0, 0x4000
	s_addc_u32 s1, s1, 0
	global_load_dword v34, v2, s[0:1]
	s_add_u32 s0, s0, 0x4000
	s_addc_u32 s1, s1, 0
	global_load_dword v35, v2, s[0:1]
	s_add_u32 s0, s0, 0x4000
	s_addc_u32 s1, s1, 0
	global_load_dword v36, v2, s[0:1]
	s_add_u32 s0, s0, 0x4000
	s_addc_u32 s1, s1, 0
	global_load_dword v37, v2, s[0:1]
	s_add_u32 s0, s0, 0x4000
	s_addc_u32 s1, s1, 0
	global_load_dword v38, v2, s[0:1]
	s_add_u32 s0, s0, 0x4000
	s_addc_u32 s1, s1, 0
	global_load_dword v39, v2, s[0:1]
	s_add_u32 s0, s0, 0x4000
	s_addc_u32 s1, s1, 0
	global_load_dword v40, v2, s[0:1]
	s_add_u32 s0, s0, 0x4000
	s_addc_u32 s1, s1, 0
	global_load_dword v41, v2, s[0:1]
	s_add_u32 s0, s0, 0x4000
	s_addc_u32 s1, s1, 0
	global_load_dword v42, v2, s[0:1]
	s_add_u32 s0, s0, 0x4000
	s_addc_u32 s1, s1, 0
	global_load_dword v43, v2, s[0:1]
	s_waitcnt vmcnt(29)
	v_max3_f32 v1, |v12|, |v13|, |v14|
	s_waitcnt vmcnt(27)
	v_max3_f32 v1, v1, |v15|, |v16|
	s_waitcnt vmcnt(25)
	v_max3_f32 v1, v1, |v17|, |v18|
	s_waitcnt vmcnt(23)
	v_max3_f32 v1, v1, |v19|, |v20|
	s_waitcnt vmcnt(21)
	v_max3_f32 v1, v1, |v21|, |v22|
	s_waitcnt vmcnt(19)
	v_max3_f32 v1, v1, |v23|, |v24|
	s_waitcnt vmcnt(17)
	v_max3_f32 v1, v1, |v25|, |v26|
	s_waitcnt vmcnt(15)
	v_max3_f32 v1, v1, |v27|, |v28|
	s_waitcnt vmcnt(13)
	v_max3_f32 v1, v1, |v29|, |v30|
	s_waitcnt vmcnt(11)
	v_max3_f32 v1, v1, |v31|, |v32|
	s_waitcnt vmcnt(9)
	v_max3_f32 v1, v1, |v33|, |v34|
	s_waitcnt vmcnt(7)
	v_max3_f32 v1, v1, |v35|, |v36|
	s_waitcnt vmcnt(5)
	v_max3_f32 v1, v1, |v37|, |v38|
	s_waitcnt vmcnt(3)
	v_max3_f32 v1, v1, |v39|, |v40|
	s_waitcnt vmcnt(1)
	v_max3_f32 v1, v1, |v41|, |v42|
	s_waitcnt vmcnt(0)
	v_max_f32_e64 v1, v1, |v43|
	v_xor_b32_e32 v2, 32, v54
	v_lshlrev_b32_e32 v2, 2, v2
	ds_bpermute_b32 v2, v2, v1
	v_readlane_b32 s2, v252, 39
	v_readlane_b32 s3, v252, 40
	s_lshl_b32 s4, s33, 7
	s_sub_u32 s4, s4, 0x100000
	s_add_u32 s2, s2, s4
	s_addc_u32 s3, s3, 0
	v_readlane_b32 s22, v252, 51
	v_readlane_b32 s23, v252, 52
	s_waitcnt lgkmcnt(0)
	v_max_f32_e32 v1, v1, v2
	v_lshlrev_b32_e32 v2, 2, v148
	s_and_saveexec_b64 s[4:5], s[22:23]
	global_store_dword v2, v1, s[2:3]
	s_or_b64 exec, exec, s[4:5]
	s_mov_b64 s[0:1], 0
; DI void p0_colmaxo_item(Frame& F, int item) {
;     const int lane = F.lane, nblk = D / 32, kb = item / nblk, nb = item % nblk, k0 = 64 * kb, n0 = 32 * nb;
;     float m = 0.f;
; #pragma unroll 8
;     for (int i = 0; i < 32; ++i) { const int kk = 2 * i + (lane >> 5); m = fmaxf(m, fabsf(F.w_out[(size_t)(k0 + kk) * D + n0 + (lane & 31)])); }
;     m = fmaxf(m, __shfl_xor(m, 32));
;     if (lane < 32) F.CMAXO[(size_t)kb * D + n0 + lane] = m;
; }
.LBB0_78:
	s_and_b64 vcc, exec, s[0:1]
	s_cbranch_vccz .LBB0_134
	s_waitcnt lgkmcnt(0)
	v_readfirstlane_b32 s2, v8
	v_readfirstlane_b32 s3, v9
	s_lshl_b32 s0, s49, 2
	s_lshl_b32 s4, s47, 13
	s_add_i32 s0, s0, s4
	s_add_u32 s0, s2, s0
	s_addc_u32 s1, s3, 0
	v_and_b32_e32 v1, 31, v148
	v_lshlrev_b32_e32 v1, 2, v1
	v_lshl_or_b32 v2, v46, 13, v1
	global_load_dword v12, v2, s[0:1]
	s_add_u32 s0, s0, 0x4000
	s_addc_u32 s1, s1, 0
	global_load_dword v13, v2, s[0:1]
	s_add_u32 s0, s0, 0x4000
	s_addc_u32 s1, s1, 0
	global_load_dword v14, v2, s[0:1]
	s_add_u32 s0, s0, 0x4000
	s_addc_u32 s1, s1, 0
	global_load_dword v15, v2, s[0:1]
	s_add_u32 s0, s0, 0x4000
	s_addc_u32 s1, s1, 0
	global_load_dword v16, v2, s[0:1]
	s_add_u32 s0, s0, 0x4000
	s_addc_u32 s1, s1, 0
	global_load_dword v17, v2, s[0:1]
	s_add_u32 s0, s0, 0x4000
	s_addc_u32 s1, s1, 0
	global_load_dword v18, v2, s[0:1]
	s_add_u32 s0, s0, 0x4000
	s_addc_u32 s1, s1, 0
	global_load_dword v19, v2, s[0:1]
	s_add_u32 s0, s0, 0x4000
	s_addc_u32 s1, s1, 0
	global_load_dword v20, v2, s[0:1]
	s_add_u32 s0, s0, 0x4000
	s_addc_u32 s1, s1, 0
	global_load_dword v21, v2, s[0:1]
	s_add_u32 s0, s0, 0x4000
	s_addc_u32 s1, s1, 0
	global_load_dword v22, v2, s[0:1]
	s_add_u32 s0, s0, 0x4000
	s_addc_u32 s1, s1, 0
	global_load_dword v23, v2, s[0:1]
	s_add_u32 s0, s0, 0x4000
	s_addc_u32 s1, s1, 0
	global_load_dword v24, v2, s[0:1]
	s_add_u32 s0, s0, 0x4000
	s_addc_u32 s1, s1, 0
	global_load_dword v25, v2, s[0:1]
	s_add_u32 s0, s0, 0x4000
	s_addc_u32 s1, s1, 0
	global_load_dword v26, v2, s[0:1]
	s_add_u32 s0, s0, 0x4000
	s_addc_u32 s1, s1, 0
	global_load_dword v27, v2, s[0:1]
	s_add_u32 s0, s0, 0x4000
	s_addc_u32 s1, s1, 0
	global_load_dword v28, v2, s[0:1]
	s_add_u32 s0, s0, 0x4000
	s_addc_u32 s1, s1, 0
	global_load_dword v29, v2, s[0:1]
	s_add_u32 s0, s0, 0x4000
	s_addc_u32 s1, s1, 0
	global_load_dword v30, v2, s[0:1]
	s_add_u32 s0, s0, 0x4000
	s_addc_u32 s1, s1, 0
	global_load_dword v31, v2, s[0:1]
	s_add_u32 s0, s0, 0x4000
	s_addc_u32 s1, s1, 0
	global_load_dword v32, v2, s[0:1]
	s_add_u32 s0, s0, 0x4000
	s_addc_u32 s1, s1, 0
	global_load_dword v33, v2, s[0:1]
	s_add_u32 s0, s0, 0x4000
	s_addc_u32 s1, s1, 0
	global_load_dword v34, v2, s[0:1]
	s_add_u32 s0, s0, 0x4000
	s_addc_u32 s1, s1, 0
	global_load_dword v35, v2, s[0:1]
	s_add_u32 s0, s0, 0x4000
	s_addc_u32 s1, s1, 0
	global_load_dword v36, v2, s[0:1]
	s_add_u32 s0, s0, 0x4000
	s_addc_u32 s1, s1, 0
	global_load_dword v37, v2, s[0:1]
	s_add_u32 s0, s0, 0x4000
	s_addc_u32 s1, s1, 0
	global_load_dword v38, v2, s[0:1]
	s_add_u32 s0, s0, 0x4000
	s_addc_u32 s1, s1, 0
	global_load_dword v39, v2, s[0:1]
	s_add_u32 s0, s0, 0x4000
	s_addc_u32 s1, s1, 0
	global_load_dword v40, v2, s[0:1]
	s_add_u32 s0, s0, 0x4000
	s_addc_u32 s1, s1, 0
	global_load_dword v41, v2, s[0:1]
	s_add_u32 s0, s0, 0x4000
	s_addc_u32 s1, s1, 0
	global_load_dword v42, v2, s[0:1]
	s_add_u32 s0, s0, 0x4000
	s_addc_u32 s1, s1, 0
	global_load_dword v43, v2, s[0:1]
	s_waitcnt vmcnt(29)
	v_max3_f32 v1, |v12|, |v13|, |v14|
	s_waitcnt vmcnt(27)
	v_max3_f32 v1, v1, |v15|, |v16|
	s_waitcnt vmcnt(25)
	v_max3_f32 v1, v1, |v17|, |v18|
	s_waitcnt vmcnt(23)
	v_max3_f32 v1, v1, |v19|, |v20|
	s_waitcnt vmcnt(21)
	v_max3_f32 v1, v1, |v21|, |v22|
	s_waitcnt vmcnt(19)
	v_max3_f32 v1, v1, |v23|, |v24|
	s_waitcnt vmcnt(17)
	v_max3_f32 v1, v1, |v25|, |v26|
	s_waitcnt vmcnt(15)
	v_max3_f32 v1, v1, |v27|, |v28|
	s_waitcnt vmcnt(13)
	v_max3_f32 v1, v1, |v29|, |v30|
	s_waitcnt vmcnt(11)
	v_max3_f32 v1, v1, |v31|, |v32|
	s_waitcnt vmcnt(9)
	v_max3_f32 v1, v1, |v33|, |v34|
	s_waitcnt vmcnt(7)
	v_max3_f32 v1, v1, |v35|, |v36|
	s_waitcnt vmcnt(5)
	v_max3_f32 v1, v1, |v37|, |v38|
	s_waitcnt vmcnt(3)
	v_max3_f32 v1, v1, |v39|, |v40|
	s_waitcnt vmcnt(1)
	v_max3_f32 v1, v1, |v41|, |v42|
	s_waitcnt vmcnt(0)
	v_max_f32_e64 v1, v1, |v43|
	v_xor_b32_e32 v2, 32, v54
	v_lshlrev_b32_e32 v2, 2, v2
	ds_bpermute_b32 v2, v2, v1
	v_readlane_b32 s2, v252, 43
	v_readlane_b32 s3, v252, 44
	s_lshl_b32 s4, s33, 7
	s_sub_u32 s4, s4, 0xc0000
	s_add_u32 s2, s2, s4
	s_addc_u32 s3, s3, 0
	v_readlane_b32 s22, v252, 51
	v_readlane_b32 s23, v252, 52
	s_waitcnt lgkmcnt(0)
	v_max_f32_e32 v1, v1, v2
	v_lshlrev_b32_e32 v2, 2, v148
	s_and_saveexec_b64 s[4:5], s[22:23]
	global_store_dword v2, v1, s[2:3]
	s_or_b64 exec, exec, s[4:5]

; DI void p0_colmax_item(Frame& F, int item) {
;     const int lane = F.lane, nblk = NWIN / 32, kb = item / nblk, nb = item % nblk, k0 = 64 * kb, n0 = 32 * nb;
;     float m = 0.f;
; #pragma unroll 8
;     for (int i = 0; i < 32; ++i) { const int kk = 2 * i + (lane >> 5); m = fmaxf(m, fabsf(__builtin_nontemporal_load(F.w_in + (size_t)(k0 + kk) * IN_COLS + n0 + (lane & 31)))); }
;     m = fmaxf(m, __shfl_xor(m, 32));
;     if (lane < 32) F.CMAXP[(size_t)kb * NWIN + n0 + lane] = m;
; }
.LBB0_135:
	s_mul_hi_i32 s0, s33, 0x2aaaaaab
	s_lshr_b32 s1, s0, 31
	s_ashr_i32 s4, s0, 5
	s_add_i32 s4, s4, s1
	s_mul_i32 s0, s4, 0xc0
	s_sub_i32 s0, s33, s0
	s_lshl_b32 s5, s0, 7
	s_mul_i32 s2, s4, 0x180800
	s_add_i32 s2, s2, s5
	v_readfirstlane_b32 s0, v10
	v_readfirstlane_b32 s1, v11
	s_add_u32 s0, s0, s2
	s_addc_u32 s1, s1, 0
	v_and_b32_e32 v1, 31, v148
	v_lshlrev_b32_e32 v1, 2, v1
	v_mul_u32_u24_e32 v2, 0x6020, v46
	v_add_u32_e32 v2, v2, v1
	s_waitcnt lgkmcnt(0)
	global_load_dword v12, v2, s[0:1] nt
	s_add_u32 s0, s0, 0xc040
	s_addc_u32 s1, s1, 0
	global_load_dword v13, v2, s[0:1] nt
	s_add_u32 s0, s0, 0xc040
	s_addc_u32 s1, s1, 0
	global_load_dword v14, v2, s[0:1] nt
	s_add_u32 s0, s0, 0xc040
	s_addc_u32 s1, s1, 0
	global_load_dword v15, v2, s[0:1] nt
	s_add_u32 s0, s0, 0xc040
	s_addc_u32 s1, s1, 0
	global_load_dword v16, v2, s[0:1] nt
	s_add_u32 s0, s0, 0xc040
	s_addc_u32 s1, s1, 0
	global_load_dword v17, v2, s[0:1] nt
	s_add_u32 s0, s0, 0xc040
	s_addc_u32 s1, s1, 0
	global_load_dword v18, v2, s[0:1] nt
	s_add_u32 s0, s0, 0xc040
	s_addc_u32 s1, s1, 0
	global_load_dword v19, v2, s[0:1] nt
	s_add_u32 s0, s0, 0xc040
	s_addc_u32 s1, s1, 0
	global_load_dword v20, v2, s[0:1] nt
	s_add_u32 s0, s0, 0xc040
	s_addc_u32 s1, s1, 0
	global_load_dword v21, v2, s[0:1] nt
	s_add_u32 s0, s0, 0xc040
	s_addc_u32 s1, s1, 0
	global_load_dword v22, v2, s[0:1] nt
	s_add_u32 s0, s0, 0xc040
	s_addc_u32 s1, s1, 0
	global_load_dword v23, v2, s[0:1] nt
	s_add_u32 s0, s0, 0xc040
	s_addc_u32 s1, s1, 0
	global_load_dword v24, v2, s[0:1] nt
	s_add_u32 s0, s0, 0xc040
	s_addc_u32 s1, s1, 0
	global_load_dword v25, v2, s[0:1] nt
	s_add_u32 s0, s0, 0xc040
	s_addc_u32 s1, s1, 0
	global_load_dword v26, v2, s[0:1] nt
	s_add_u32 s0, s0, 0xc040
	s_addc_u32 s1, s1, 0
	global_load_dword v27, v2, s[0:1] nt
	s_add_u32 s0, s0, 0xc040
	s_addc_u32 s1, s1, 0
	global_load_dword v28, v2, s[0:1] nt
	s_add_u32 s0, s0, 0xc040
	s_addc_u32 s1, s1, 0
	global_load_dword v29, v2, s[0:1] nt
	s_add_u32 s0, s0, 0xc040
	s_addc_u32 s1, s1, 0
	global_load_dword v30, v2, s[0:1] nt
	s_add_u32 s0, s0, 0xc040
	s_addc_u32 s1, s1, 0
	global_load_dword v31, v2, s[0:1] nt
	s_add_u32 s0, s0, 0xc040
	s_addc_u32 s1, s1, 0
	global_load_dword v32, v2, s[0:1] nt
	s_add_u32 s0, s0, 0xc040
	s_addc_u32 s1, s1, 0
	global_load_dword v33, v2, s[0:1] nt
	s_add_u32 s0, s0, 0xc040
	s_addc_u32 s1, s1, 0
	global_load_dword v34, v2, s[0:1] nt
	s_add_u32 s0, s0, 0xc040
	s_addc_u32 s1, s1, 0
	global_load_dword v35, v2, s[0:1] nt
	s_add_u32 s0, s0, 0xc040
	s_addc_u32 s1, s1, 0
	global_load_dword v36, v2, s[0:1] nt
	s_add_u32 s0, s0, 0xc040
	s_addc_u32 s1, s1, 0
	global_load_dword v37, v2, s[0:1] nt
	s_add_u32 s0, s0, 0xc040
	s_addc_u32 s1, s1, 0
	global_load_dword v38, v2, s[0:1] nt
	s_add_u32 s0, s0, 0xc040
	s_addc_u32 s1, s1, 0
	global_load_dword v39, v2, s[0:1] nt
	s_add_u32 s0, s0, 0xc040
	s_addc_u32 s1, s1, 0
	global_load_dword v40, v2, s[0:1] nt
	s_add_u32 s0, s0, 0xc040
	s_addc_u32 s1, s1, 0
	global_load_dword v41, v2, s[0:1] nt
	s_add_u32 s0, s0, 0xc040
	s_addc_u32 s1, s1, 0
	global_load_dword v42, v2, s[0:1] nt
	s_add_u32 s0, s0, 0xc040
	s_addc_u32 s1, s1, 0
	global_load_dword v43, v2, s[0:1] nt
	s_waitcnt vmcnt(29)
	v_max3_f32 v1, |v12|, |v13|, |v14|
	s_waitcnt vmcnt(27)
	v_max3_f32 v1, v1, |v15|, |v16|
	s_waitcnt vmcnt(25)
	v_max3_f32 v1, v1, |v17|, |v18|
	s_waitcnt vmcnt(23)
	v_max3_f32 v1, v1, |v19|, |v20|
	s_waitcnt vmcnt(21)
	v_max3_f32 v1, v1, |v21|, |v22|
	s_waitcnt vmcnt(19)
	v_max3_f32 v1, v1, |v23|, |v24|
	s_waitcnt vmcnt(17)
	v_max3_f32 v1, v1, |v25|, |v26|
	s_waitcnt vmcnt(15)
	v_max3_f32 v1, v1, |v27|, |v28|
	s_waitcnt vmcnt(13)
	v_max3_f32 v1, v1, |v29|, |v30|
	s_waitcnt vmcnt(11)
	v_max3_f32 v1, v1, |v31|, |v32|
	s_waitcnt vmcnt(9)
	v_max3_f32 v1, v1, |v33|, |v34|
	s_waitcnt vmcnt(7)
	v_max3_f32 v1, v1, |v35|, |v36|
	s_waitcnt vmcnt(5)
	v_max3_f32 v1, v1, |v37|, |v38|
	s_waitcnt vmcnt(3)
	v_max3_f32 v1, v1, |v39|, |v40|
	s_waitcnt vmcnt(1)
	v_max3_f32 v1, v1, |v41|, |v42|
	s_waitcnt vmcnt(0)
	v_max_f32_e64 v1, v1, |v43|
	v_xor_b32_e32 v2, 32, v54
	v_lshlrev_b32_e32 v2, 2, v2
	ds_bpermute_b32 v2, v2, v1
	v_readlane_b32 s2, v252, 41
	v_readlane_b32 s3, v252, 42
	s_mul_i32 s4, s4, 0x6000
	s_add_i32 s4, s4, s5
	s_add_u32 s2, s2, s4
	s_addc_u32 s3, s3, 0
	v_readlane_b32 s22, v252, 51
	v_readlane_b32 s23, v252, 52
	s_waitcnt lgkmcnt(0)
	v_max_f32_e32 v1, v1, v2
	v_lshlrev_b32_e32 v2, 2, v148
	s_and_saveexec_b64 s[4:5], s[22:23]
	global_store_dword v2, v1, s[2:3]
	s_or_b64 exec, exec, s[4:5]
	s_branch .LBB0_19
